# v16 + second half of layer-0 expert-weight conversion deferred from prologue P0 to the 128 idle workgroups of the kv-GEMM phase P1
# baseline (speedup 1.0000x reference)
; #define CIN(i) ((const float*)*(const GAS float* const __attribute__((address_space(4)))*)(C.ka + 8 * (i)))
; DI void convert_layer_item(const Ctx& C, int l, int it, int lane) {
;     if (it < LI_WIN) { const int kb = it / 96, nb = it % 96, n0 = nb * 64;
;         if (l >= L8) { tr_item<true>(CIN(I_WIN) + (size_t)l * D * INW, INW, kb * 64, n0, CIN(I_NMIX) + l * D, W8S, (unsigned char*)(WSP(bf16_t, WS_WIN) + (size_t)l * INW * D), D, n0, lane); return; }
;         const float ns = (n0 < 1024) ? SC_A : ((n0 >= 3072 && n0 < 4096) ? SC_B : 1.f);
;         tr_item(CIN(I_WIN) + (size_t)l * D * INW, INW, kb * 64, n0, CIN(I_NMIX) + l * D, ns, WSP(bf16_t, WS_WIN) + (size_t)l * INW * D, D, n0, lane); return; }
;     it -= LI_WIN;
;     if (it < LI_WOUT) { const int kb = it / 32, nb = it % 32;
;         if (l >= L8B) { tr_item<true>(CIN(I_WOUT) + (size_t)l * D * D, D, kb * 64, nb * 64, nullptr, W8S, (unsigned char*)(WSP(bf16_t, WS_WOUT) + (size_t)l * D * D), D, nb * 64, lane); return; }
;         tr_item(CIN(I_WOUT) + (size_t)l * D * D, D, kb * 64, nb * 64, nullptr, 1.f, WSP(bf16_t, WS_WOUT) + (size_t)l * D * D, D, nb * 64, lane); return; }
;     it -= LI_WOUT;
;     if (it < LI_W13) { const int le = l * NE + it / 128, r = it % 128, kb = r / 4, nb = r % 4;
;         bf16_t* dst = WSP(bf16_t, WS_W13) + (size_t)le * 512 * D; const int dr = (nb >> 1) * 256 + (nb & 1) * 64;
;         if (l >= L8M) { unsigned char* d8 = (unsigned char*)(WSP(bf16_t, WS_W13) + (size_t)l * NE * 512 * D) + (size_t)(it / 128) * 512 * D;
;             tr_item<true>(CIN(I_W1) + (size_t)le * D * DE, DE, kb * 64, nb * 64, CIN(I_NFFN) + l * D, W8S, d8, D, dr, lane);
;             tr_item<true>(CIN(I_W3) + (size_t)le * D * DE, DE, kb * 64, nb * 64, CIN(I_NFFN) + l * D, W8S, d8, D, dr + 128, lane); return; }
;         tr_item(CIN(I_W1) + (size_t)le * D * DE, DE, kb * 64, nb * 64, CIN(I_NFFN) + l * D, 1.f, dst, D, dr, lane);
;         tr_item(CIN(I_W3) + (size_t)le * D * DE, DE, kb * 64, nb * 64, CIN(I_NFFN) + l * D, 1.f, dst, D, dr + 128, lane); return; }
;     it -= LI_W13;
;     { const int le = l * NE + it / 128, r = it % 128, kb = r / 32, nb = r % 32;
; DI void phase_prologue(const Ctx& C) {
;     const int gw = C.gw, ngw = C.ngw, lane = C.lane;
;     for (int it = gw; it < LAYER_ITEMS; it += ngw) convert_layer_item(C, 0, it, lane);
.LBB0_5:
	s_or_b64 exec, exec, s[4:5]
	s_lshr_b32 s13, s12, 6
	s_lshl_b32 s3, s2, 3
	s_add_i32 s94, s13, s3
	s_lshl_b32 s82, s33, 3
	s_cmp_lt_i32 s92, 1
	s_cselect_b64 s[4:5], -1, 0
	s_cmp_gt_i32 s93, 0
	s_cselect_b64 s[6:7], -1, 0
	s_and_b64 s[4:5], s[4:5], s[6:7]
	s_andn2_b64 vcc, exec, s[4:5]
	s_mov_b64 s[4:5], s[42:43]
	v_writelane_b32 v251, s4, 2
	s_nop 1
	v_writelane_b32 v251, s5, 3
	s_cbranch_vccnz .LBB0_163
s_mov_b32 s100, 0x17ff
s_mov_b32 s101, 0
.Lp0_conv_entry:
	s_mov_b32 s3, 0
	s_mov_b64 s[4:5], s[42:43]
	s_mov_b32 s7, 0
	v_mbcnt_lo_u32_b32 v0, -1, s3
	v_writelane_b32 v251, s4, 2
	v_mbcnt_hi_u32_b32 v64, -1, v0
	s_cmpk_gt_i32 s94, 0x2fff
	v_writelane_b32 v251, s5, 3
	v_and_b32_e32 v66, -16, v64
	s_cbranch_scc1 .LBB0_29
	v_readlane_b32 s4, v251, 2
	v_readlane_b32 s5, v251, 3
	s_add_u32 s3, s4, 0x42000000
	s_addc_u32 s19, s5, 0
	s_add_u32 s26, s4, 0x32000000
	s_addc_u32 s27, s5, 0
	s_add_u32 s14, s4, 0x28000000
	v_lshlrev_b32_e32 v0, 2, v64
	s_addc_u32 s15, s5, 0
	v_and_b32_e32 v68, 60, v0
	s_add_u32 s16, s4, 0x22000000
	v_mov_b32_e32 v71, 0
	v_ashrrev_i32_e32 v67, 31, v66
	s_addc_u32 s17, s5, 0
	s_lshl_b32 s28, s94, 6
	s_lshl_b32 s29, s82, 6
	s_lshl_b32 s30, s94, 1
	s_lshl_b32 s31, s82, 1
	s_lshl_b32 s34, s94, 7
	s_lshl_b32 s35, s82, 7
	s_lshl_b32 s36, s94, 4
	s_lshl_b32 s37, s82, 4
	s_movk_i32 s38, 0x2000
	s_movk_i32 s39, 0x4000
	s_movk_i32 s44, 0x6000
	s_mov_b32 s45, 0x8000
	s_mov_b32 s46, 0xa000
	s_mov_b32 s47, 0xc000
	s_mov_b32 s48, 0xe000
	s_mov_b32 s49, 0x10000
	s_mov_b32 s51, 0x12000
	s_mov_b32 s52, 0x14000
	s_mov_b32 s53, 0x16000
	s_mov_b32 s54, 0x18000
	s_mov_b32 s55, 0x1a000
	s_mov_b32 s56, 0x1c000
	s_mov_b32 s57, 0x1e000
	s_mov_b32 s18, 0x42800000
	s_movk_i32 s60, 0x1000
	s_movk_i32 s61, 0x3000
	s_mov_b64 s[20:21], 0x40000
	s_mov_b32 s62, 0x41000
	s_mov_b32 s63, 0x24000
	s_mov_b32 s64, 0x2a000
	s_mov_b32 s65, 0x30000
	s_mov_b32 s66, 0x36000
	s_mov_b32 s67, 0x3c000
	s_mov_b32 s68, 0x42000
	s_mov_b32 s69, 0x48000
	v_lshlrev_b32_e32 v70, 2, v68
	v_mov_b32_e32 v65, 0x3e38aa3b
	v_mov_b32_e32 v69, 0x3e0293ee
	s_mov_b32 s70, s94
	s_branch .LBB0_10

; DI void phase_prologue(const Ctx& C) {
;     ...
;     for (int it = gw; it < LAYER_ITEMS; it += ngw) convert_layer_item(C, 0, it, lane);
.LBB0_9:
	s_add_i32 s70, s70, s82
	s_add_i32 s28, s28, s29
	s_add_i32 s30, s30, s31
	s_add_i32 s34, s34, s35
	s_add_i32 s36, s36, s37
	s_cmp_gt_i32 s70, s100
	s_cbranch_scc1 .LBB0_29

; #define CIN(i) ((const float*)*(const GAS float* const __attribute__((address_space(4)))*)(C.ka + 8 * (i)))
; DI void phase_prologue(const Ctx& C) {
;     ...
;     for (int it = gw; it < LAYER_ITEMS; it += ngw) convert_layer_item(C, 0, it, lane);
;     for (int it = gw; it < NL * 2048; it += ngw) { const int l = it / 2048, r = it % 2048, kb = r / 64, nb = r % 64;
;         tr_item<true>(CIN(I_WXKV) + (size_t)l * D * 4096, 4096, kb * 64, nb * 64, CIN(I_NMEM) + l * D, W8S, WSP(unsigned char, WS_WKV) + (size_t)l * 4096 * D, D, nb * 64, lane); }
.LBB0_29:
s_cmp_eq_u32 s101, 1
s_cbranch_scc1 .Lp1_conv_ret
	s_cmpk_gt_i32 s94, 0x1fff
	s_cbranch_scc1 .LBB0_35
	s_load_dwordx2 s[6:7], s[0:1], 0x50
	s_load_dwordx2 s[8:9], s[0:1], 0x60
	v_readlane_b32 s4, v251, 2
	v_readlane_b32 s5, v251, 3
	s_add_u32 s3, s4, 0x2c000000
	s_addc_u32 s11, s5, 0
	s_waitcnt lgkmcnt(0)
	s_cmp_lg_u64 s[6:7], 0
	v_lshlrev_b32_e32 v0, 2, v64
	s_cselect_b64 s[4:5], -1, 0
	v_and_b32_e32 v68, 60, v0
	v_cndmask_b32_e64 v0, 0, 1, s[4:5]
	v_mov_b32_e32 v71, 0
	v_ashrrev_i32_e32 v67, 31, v66
	v_lshlrev_b32_e32 v70, 2, v68
	s_movk_i32 s20, 0x4000
	s_mov_b32 s21, 0x8000
	s_mov_b32 s22, 0xc000
	s_mov_b32 s23, 0x10000
	s_mov_b32 s24, 0x14000
	s_mov_b32 s25, 0x18000
	s_mov_b32 s26, 0x1c000
	s_mov_b32 s27, 0x20000
	s_mov_b32 s28, 0x24000
	s_mov_b32 s29, 0x28000
	s_mov_b32 s30, 0x2c000
	s_mov_b32 s31, 0x30000
	v_cmp_ne_u32_e64 s[4:5], 1, v0
	s_mov_b32 s10, 0x42800000
	s_movk_i32 s34, 0x1000
	s_mov_b32 s35, s94
	s_branch .LBB0_33

; #define PH_END   if (p + 1 < hi) xcd_barrier(bar, C.tid); else __syncthreads(); } ++p;
; DI void phase_prologue(const Ctx& C) {
;     ...
;     for (int it = gw; it < LAYER_ITEMS; it += ngw) convert_layer_item(C, 0, it, lane);
; __global__ void __launch_bounds__(NTHREADS, 2) mk_fwd(Args args) {
;     ...
;     PH_BEGIN
;         pg8::MultiOrder S{(const char*)WSP(unsigned char, WS_MEMB), (const char*)WSP(unsigned char, WS_WKV), 0, 0, 0, (size_t)4096 * D, 0, 0, 0, 0, 0, 2, 16, NL, D / 2, D / 2, XCD_G(128), XCD_C(128)};
;         pg8::EpiStore<2, false, true> E{WSP(bf16_t, WS_KVB), (size_t)MT * 4096, 0, 0, 0, 4096, WSP(float, WS_RMEM), 0, 1.f / W8S};
;         pg8::gemm_phase<pg8::EpiStore<2, false, true>, pg8::MultiOrder, true, false, true>(C.lds, C.tid, D / 2, D / 2, D / 2, S, E);
;     PH_END
.Lp1_detour:
	s_add_i32 s94, s94, 0x1400
	s_movk_i32 s82, 0x400
	s_mov_b32 s100, 0x2fff
	s_mov_b32 s101, 1
	s_branch .Lp0_conv_entry
.Lp1_conv_ret:
	s_sub_i32 s94, s94, 0x1400
	s_lshl_b32 s82, s33, 3
	s_mov_b32 s101, 0

; __global__ void __launch_bounds__(NTHREADS, 2) mk_fwd(Args args) {
	.amdhsa_kernel _Z6mk_fwd4Args
		.amdhsa_group_segment_fixed_size 0
		.amdhsa_private_segment_fixed_size 0
		.amdhsa_kernarg_size 464
		.amdhsa_user_sgpr_count 2
		.amdhsa_user_sgpr_dispatch_ptr 0
		.amdhsa_user_sgpr_queue_ptr 0
		.amdhsa_user_sgpr_kernarg_segment_ptr 1
		.amdhsa_user_sgpr_dispatch_id 0
		.amdhsa_user_sgpr_kernarg_preload_length 0
		.amdhsa_user_sgpr_kernarg_preload_offset 0
		.amdhsa_user_sgpr_private_segment_size 0
		.amdhsa_uses_dynamic_stack 0
		.amdhsa_enable_private_segment 0
		.amdhsa_system_sgpr_workgroup_id_x 1
		.amdhsa_system_sgpr_workgroup_id_y 0
		.amdhsa_system_sgpr_workgroup_id_z 0
		.amdhsa_system_sgpr_workgroup_info 0
		.amdhsa_system_vgpr_workitem_id 0
		.amdhsa_next_free_vgpr 256
		.amdhsa_next_free_sgpr 102
		.amdhsa_accum_offset 256
		.amdhsa_reserve_vcc 1
		.amdhsa_float_round_mode_32 0
		.amdhsa_float_round_mode_16_64 0
		.amdhsa_float_denorm_mode_32 3
		.amdhsa_float_denorm_mode_16_64 3
		.amdhsa_dx10_clamp 1
		.amdhsa_ieee_mode 1
		.amdhsa_fp16_overflow 0
		.amdhsa_tg_split 0
		.amdhsa_exception_fp_ieee_invalid_op 0
		.amdhsa_exception_fp_denorm_src 0
		.amdhsa_exception_fp_ieee_div_zero 0
		.amdhsa_exception_fp_ieee_overflow 0
		.amdhsa_exception_fp_ieee_underflow 0
		.amdhsa_exception_fp_ieee_inexact 0
		.amdhsa_exception_int_div_zero 0
	.end_amdhsa_kernel

; __global__ void __launch_bounds__(NTHREADS, 2) mk_fwd(Args args) {
amdhsa.kernels:
  - .agpr_count:     0
    .args:
      - .offset:         0
        .size:           208
        .value_kind:     by_value
      - .offset:         208
        .size:           4
        .value_kind:     hidden_block_count_x
      - .offset:         212
        .size:           4
        .value_kind:     hidden_block_count_y
      - .offset:         216
        .size:           4
        .value_kind:     hidden_block_count_z
      - .offset:         220
        .size:           2
        .value_kind:     hidden_group_size_x
      - .offset:         222
        .size:           2
        .value_kind:     hidden_group_size_y
      - .offset:         224
        .size:           2
        .value_kind:     hidden_group_size_z
      - .offset:         226
        .size:           2
        .value_kind:     hidden_remainder_x
      - .offset:         228
        .size:           2
        .value_kind:     hidden_remainder_y
      - .offset:         230
        .size:           2
        .value_kind:     hidden_remainder_z
      - .offset:         248
        .size:           8
        .value_kind:     hidden_global_offset_x
      - .offset:         256
        .size:           8
        .value_kind:     hidden_global_offset_y
      - .offset:         264
        .size:           8
        .value_kind:     hidden_global_offset_z
      - .offset:         272
        .size:           2
        .value_kind:     hidden_grid_dims
      - .offset:         328
        .size:           4
        .value_kind:     hidden_dynamic_lds_size
    .group_segment_fixed_size: 0
    .kernarg_segment_align: 8
    .kernarg_segment_size: 464
    .language:       OpenCL C
    .language_version:
      - 2
      - 0
    .max_flat_workgroup_size: 512
    .name:           _Z6mk_fwd4Args
    .private_segment_fixed_size: 0
    .sgpr_count:     108
    .sgpr_spill_count: 349
    .symbol:         _Z6mk_fwd4Args.kd
    .uniform_work_group_size: 1
    .uses_dynamic_stack: false
    .vgpr_count:     256
    .vgpr_spill_count: 0
    .wavefront_size: 64
